# attention pass prologue: the four Q loads issued together into free registers and the K/V LDS-DMAs issued before waiting on Q (counted vmcnt) instead of four serialized load/wait round trips; plus pre
# baseline (speedup 1.0000x reference)
; __device__ __forceinline__ unsigned cvt_pk_bf16(float lo, float hi) { unsigned r; asm volatile("v_cvt_pk_bf16_f32 %0, %1, %2" : "=v"(r) : "v"(lo), "v"(hi)); return r; }
; __device__ __forceinline__ float bf_lo(unsigned w) { return __uint_as_float(w << 16); }
; __device__ __forceinline__ float bf_hi(unsigned w) { return __uint_as_float(w & 0xffff0000u); }
;     __device__ __forceinline__ bf16_t* proj() const { return (bf16_t*)(ws + WS_PROJ); }
; #define AT_DMA_K(j, so) do { const char* _p = pb + (size_t)__builtin_amdgcn_readfirstlane(AT_ROW(j)) * (INW * 2); \
;         __builtin_amdgcn_global_load_lds((const unsigned*)(_p + dK), (LAS unsigned*)(lds + (so) + SHM_V + widu * 1024), 16, 0, 0); } while (0)
; #define AT_DMA_V(j, so) do { const char* _p = pb + (size_t)__builtin_amdgcn_readfirstlane(AT_ROW(j)) * (INW * 2); \
;         __builtin_amdgcn_global_load_lds((const unsigned*)(_p + dV0), (LAS unsigned*)(lds + (so) + widu * 2048), 16, 0, 0); \
;         __builtin_amdgcn_global_load_lds((const unsigned*)(_p + dV1), (LAS unsigned*)(lds + (so) + widu * 2048 + 1024), 16, 0, 0); } while (0)
; template <bool ROBUST>
; __device__ __forceinline__ bool attn_pass(const bf16_t* __restrict__ proj, LAS char* lds, int qrow0, int ctxrow0, int latrow0, int NT, int h, int comp, f32x16 (&o)[4]) {
;     ...
;     { const bf16_t* Qw = proj + (size_t)(qrow0 + wid * 32 + r32) * INW + C_Q + h * 128 + comp * 64 + hi * 8;
; #pragma unroll
;       for (int d0 = 0; d0 < 4; ++d0) {
;           const u32x4 w = *(const u32x4*)(Qw + d0 * 16); constexpr float C = SCALE * 1.4426950408889634f; u32x4 s;
;           s.x = cvt_pk_bf16(bf_lo(w.x) * C, bf_hi(w.x) * C); s.y = cvt_pk_bf16(bf_lo(w.y) * C, bf_hi(w.y) * C); s.z = cvt_pk_bf16(bf_lo(w.z) * C, bf_hi(w.z) * C); s.w = cvt_pk_bf16(bf_lo(w.w) * C, bf_hi(w.w) * C);
;           qr[d0] = *reinterpret_cast<bf16x8*>(&s); } }
;     ...
;     AT_DMA_K(0, 0); AT_DMA_V(0, 0); AT_DMA_K(1, SLOT); AT_DMA_V(1, SLOT); AT_DMA_K(2, 2 * SLOT);
;     asm volatile("s_waitcnt vmcnt(4)" ::: "memory"); __syncthreads();
.LBB0_348:
	v_mov_b32_e32 v195, v0
	v_mov_b32_e32 v171, v147
	v_ashrrev_i32_e32 v8, 6, v195
	v_and_b32_e32 v194, 31, v195
	v_lshlrev_b32_e32 v2, 5, v8
	v_add3_u32 v2, v194, s30, v2
	v_ashrrev_i32_e32 v3, 31, v2
	v_lshlrev_b64 v[2:3], 13, v[2:3]
	v_bfe_u32 v4, v195, 5, 1
	v_lshl_add_u64 v[2:3], s[68:69], 0, v[2:3]
	v_lshl_add_u64 v[2:3], s[76:77], 1, v[2:3]
	v_lshlrev_b32_e32 v170, 4, v4
	v_lshl_add_u64 v[2:3], v[2:3], 0, v[170:171]
	global_load_dwordx4 v[48:51], v[2:3], off
	global_load_dwordx4 v[36:39], v[2:3], off offset:32
	global_load_dwordx4 v[40:43], v[2:3], off offset:64
	global_load_dwordx4 v[44:47], v[2:3], off offset:96
	v_lshlrev_b32_e32 v34, 3, v195
	s_ashr_i32 s67, s66, 31
	s_lshl_b64 s[24:25], s[66:67], 13
	v_readfirstlane_b32 s40, v8
	s_add_u32 s8, s48, s24
	s_addc_u32 s9, s49, s25
	s_lshl_b32 s1, s40, 10
	s_add_i32 s78, s1, 0
	s_add_i32 s0, s78, 0x4000
	s_mov_b32 m0, s0
	v_mov_b32_e32 v173, v147
	s_add_i32 s79, s78, s1
	s_add_i32 s7, s79, 0x400
	v_cmp_eq_u32_e32 vcc, 0, v195
	v_lshlrev_b32_e32 v2, 3, v8
	v_bfe_u32 v3, v195, 2, 3
	v_or_b32_e32 v3, v2, v3
	v_and_b32_e32 v4, 32, v195
	v_lshl_or_b32 v3, v3, 12, v4
	v_and_b32_e32 v4, 24, v34
	v_or3_b32 v3, v3, v4, s31
	v_lshlrev_b32_e32 v172, 1, v3
	v_bfe_u32 v3, v195, 3, 3
	v_or_b32_e32 v2, v2, v3
	v_lshl_or_b32 v3, v2, 12, s31
	v_lshrrev_b32_e32 v2, 1, v2
	v_xor_b32_e32 v2, v2, v195
	v_lshlrev_b32_e32 v2, 4, v2
	v_or_b32_e32 v3, s76, v3
	v_and_b32_e32 v2, 0x70, v2
	v_lshl_or_b32 v146, v3, 1, v2
	v_lshl_add_u64 v[2:3], s[8:9], 0, v[146:147]
	v_lshl_add_u64 v[2:3], v[2:3], 0, s[10:11]
	global_load_lds_dwordx4 v[2:3], off
	v_lshl_add_u64 v[2:3], s[8:9], 0, v[172:173]
	v_lshl_add_u64 v[4:5], v[2:3], 0, s[38:39]
	s_mov_b32 m0, s79
	s_add_u32 s8, s8, 0x80000
	global_load_lds_dwordx4 v[4:5], off
	v_lshl_add_u64 v[2:3], v[2:3], 0, s[4:5]
	s_mov_b32 m0, s7
	s_addc_u32 s9, s9, 0
	global_load_lds_dwordx4 v[2:3], off
	v_lshl_add_u64 v[2:3], s[8:9], 0, v[146:147]
	s_add_i32 s42, s78, 0xa000
	v_lshl_add_u64 v[2:3], v[2:3], 0, s[10:11]
	s_mov_b32 m0, s42
	s_ashr_i32 s71, s70, 31
	global_load_lds_dwordx4 v[2:3], off
	v_lshl_add_u64 v[2:3], s[8:9], 0, v[172:173]
	s_add_i32 s1, s79, 0x6000
	s_add_i32 s2, s79, 0x6400
	s_lshl_b64 s[8:9], s[70:71], 13
	v_lshl_add_u64 v[4:5], v[2:3], 0, s[38:39]
	s_mov_b32 m0, s1
	s_add_u32 s8, s48, s8
	global_load_lds_dwordx4 v[4:5], off
	v_lshl_add_u64 v[2:3], v[2:3], 0, s[4:5]
	s_mov_b32 m0, s2
	s_addc_u32 s9, s49, s9
	global_load_lds_dwordx4 v[2:3], off
	v_lshl_add_u64 v[2:3], s[8:9], 0, v[146:147]
	s_add_i32 s80, s78, 0x10000
	v_lshl_add_u64 v[2:3], v[2:3], 0, s[10:11]
	s_mov_b32 m0, s80
	s_nop 0
	global_load_lds_dwordx4 v[2:3], off
	s_waitcnt vmcnt(10)
	v_lshlrev_b32_e32 v9, 16, v48
	v_and_b32_e32 v4, 0xffff0000, v48
	v_mul_f32_e32 v4, 0x3e38aa3b, v4
	v_mul_f32_e32 v9, 0x3e38aa3b, v9
	v_cvt_pk_bf16_f32 v148, v9, v4
	v_lshlrev_b32_e32 v4, 16, v49
	v_and_b32_e32 v5, 0xffff0000, v49
	v_mul_f32_e32 v4, 0x3e38aa3b, v4
	v_mul_f32_e32 v5, 0x3e38aa3b, v5
	v_cvt_pk_bf16_f32 v149, v4, v5
	v_lshlrev_b32_e32 v4, 16, v50
	v_and_b32_e32 v5, 0xffff0000, v50
	v_mul_f32_e32 v4, 0x3e38aa3b, v4
	v_mul_f32_e32 v5, 0x3e38aa3b, v5
	v_cvt_pk_bf16_f32 v150, v4, v5
	v_lshlrev_b32_e32 v4, 16, v51
	v_and_b32_e32 v5, 0xffff0000, v51
	v_mul_f32_e32 v4, 0x3e38aa3b, v4
	v_mul_f32_e32 v5, 0x3e38aa3b, v5
	v_cvt_pk_bf16_f32 v151, v4, v5
	s_waitcnt vmcnt(9)
	v_lshlrev_b32_e32 v9, 16, v36
	v_and_b32_e32 v4, 0xffff0000, v36
	v_mul_f32_e32 v4, 0x3e38aa3b, v4
	v_mul_f32_e32 v9, 0x3e38aa3b, v9
	v_cvt_pk_bf16_f32 v152, v9, v4
	v_lshlrev_b32_e32 v4, 16, v37
	v_and_b32_e32 v5, 0xffff0000, v37
	v_mul_f32_e32 v4, 0x3e38aa3b, v4
	v_mul_f32_e32 v5, 0x3e38aa3b, v5
	v_cvt_pk_bf16_f32 v153, v4, v5
	v_lshlrev_b32_e32 v4, 16, v38
	v_and_b32_e32 v5, 0xffff0000, v38
	v_mul_f32_e32 v4, 0x3e38aa3b, v4
	v_mul_f32_e32 v5, 0x3e38aa3b, v5
	v_cvt_pk_bf16_f32 v154, v4, v5
	v_lshlrev_b32_e32 v4, 16, v39
	v_and_b32_e32 v5, 0xffff0000, v39
	v_mul_f32_e32 v4, 0x3e38aa3b, v4
	v_mul_f32_e32 v5, 0x3e38aa3b, v5
	v_cvt_pk_bf16_f32 v155, v4, v5
	s_waitcnt vmcnt(8)
	v_lshlrev_b32_e32 v9, 16, v40
	v_and_b32_e32 v4, 0xffff0000, v40
	v_mul_f32_e32 v4, 0x3e38aa3b, v4
	v_mul_f32_e32 v9, 0x3e38aa3b, v9
	v_cvt_pk_bf16_f32 v156, v9, v4
	v_lshlrev_b32_e32 v4, 16, v41
	v_and_b32_e32 v5, 0xffff0000, v41
	v_mul_f32_e32 v4, 0x3e38aa3b, v4
	v_mul_f32_e32 v5, 0x3e38aa3b, v5
	v_cvt_pk_bf16_f32 v157, v4, v5
	v_lshlrev_b32_e32 v4, 16, v42
	v_and_b32_e32 v5, 0xffff0000, v42
	v_mul_f32_e32 v4, 0x3e38aa3b, v4
	v_mul_f32_e32 v5, 0x3e38aa3b, v5
	v_cvt_pk_bf16_f32 v158, v4, v5
	v_lshlrev_b32_e32 v4, 16, v43
	v_and_b32_e32 v5, 0xffff0000, v43
	v_mul_f32_e32 v4, 0x3e38aa3b, v4
	v_mul_f32_e32 v5, 0x3e38aa3b, v5
	v_cvt_pk_bf16_f32 v159, v4, v5
	s_waitcnt vmcnt(7)
	v_lshlrev_b32_e32 v9, 16, v44
	v_and_b32_e32 v4, 0xffff0000, v44
	v_mul_f32_e32 v4, 0x3e38aa3b, v4
	v_mul_f32_e32 v9, 0x3e38aa3b, v9
	v_cvt_pk_bf16_f32 v160, v9, v4
	v_lshlrev_b32_e32 v4, 16, v45
	v_and_b32_e32 v5, 0xffff0000, v45
	v_mul_f32_e32 v4, 0x3e38aa3b, v4
	v_mul_f32_e32 v5, 0x3e38aa3b, v5
	v_cvt_pk_bf16_f32 v161, v4, v5
	v_lshlrev_b32_e32 v4, 16, v46
	v_and_b32_e32 v5, 0xffff0000, v46
	v_mul_f32_e32 v4, 0x3e38aa3b, v4
	v_mul_f32_e32 v5, 0x3e38aa3b, v5
	v_cvt_pk_bf16_f32 v162, v4, v5
	v_lshlrev_b32_e32 v4, 16, v47
	v_and_b32_e32 v5, 0xffff0000, v47
	v_mul_f32_e32 v4, 0x3e38aa3b, v4
	v_mul_f32_e32 v5, 0x3e38aa3b, v5
	v_cvt_pk_bf16_f32 v163, v4, v5
	s_waitcnt vmcnt(4)
	s_waitcnt vmcnt(0) lgkmcnt(0)
	s_barrier
; #define LAS __attribute__((address_space(3)))
; #define AT_DMA_K(j, so) do { const char* _p = pb + (size_t)__builtin_amdgcn_readfirstlane(AT_ROW(j)) * (INW * 2); \
;         __builtin_amdgcn_global_load_lds((const unsigned*)(_p + dK), (LAS unsigned*)(lds + (so) + SHM_V + widu * 1024), 16, 0, 0); } while (0)
; #define AT_DMA_V(j, so) do { const char* _p = pb + (size_t)__builtin_amdgcn_readfirstlane(AT_ROW(j)) * (INW * 2); \
;         __builtin_amdgcn_global_load_lds((const unsigned*)(_p + dV0), (LAS unsigned*)(lds + (so) + widu * 2048), 16, 0, 0); \
;         __builtin_amdgcn_global_load_lds((const unsigned*)(_p + dV1), (LAS unsigned*)(lds + (so) + widu * 2048 + 1024), 16, 0, 0); } while (0)
; __device__ __forceinline__ void qkt(f32x16& p0, f32x16& p1, const LAS char* Ks, const bf16x8* qr, int r32, int hi, float init) {
; #pragma unroll
;     for (int r = 0; r < 16; ++r) { p0[r] = init; p1[r] = init; }
; #pragma unroll
;     for (int d0 = 0; d0 < 4; ++d0) { const int cb = (d0 * 16 + hi * 8) * 2;
;         const bf16x8 b0 = *(const LAS bf16x8*)(Ks + AT_KSWZ(r32, cb));
;         const bf16x8 b1 = *(const LAS bf16x8*)(Ks + AT_KSWZ(32 + r32, cb));
;         p0 = __builtin_amdgcn_mfma_f32_32x32x16_bf16(b0, qr[d0], p0, 0, 0, 0);
;         p1 = __builtin_amdgcn_mfma_f32_32x32x16_bf16(b1, qr[d0], p1, 0, 0, 0); }
; template <bool ROBUST>
; __device__ __forceinline__ bool attn_pass(const bf16_t* __restrict__ proj, LAS char* lds, int qrow0, int ctxrow0, int latrow0, int NT, int h, int comp, f32x16 (&o)[4]) {
;     ...
;     AT_DMA_K(0, 0); AT_DMA_V(0, 0); AT_DMA_K(1, SLOT); AT_DMA_V(1, SLOT); AT_DMA_K(2, 2 * SLOT);
;     asm volatile("s_waitcnt vmcnt(4)" ::: "memory"); __syncthreads();
;     if (tid == 0) *(LAS int*)(lds + OFF_FLAG) = 0;
;     qkt(pA0, pA1, lds + SHM_V, qr, r32, hi, 0.f); partialSM<true>(pA0, pA1, m_reg, alA);
;     asm volatile("s_waitcnt vmcnt(1)" ::: "memory"); __syncthreads();
	s_and_saveexec_b64 s[8:9], vcc
	v_mov_b32_e32 v2, s16
	ds_write_b32 v2, v147
	s_or_b64 exec, exec, s[8:9]
	v_lshlrev_b32_e32 v35, 7, v194
	v_lshlrev_b32_e32 v2, 3, v194
	v_and_b32_e32 v48, 0x70, v2
	v_add_u32_e32 v49, 0, v35
	v_xad_u32 v6, v170, v48, v49
	ds_read_b128 v[2:5], v6 offset:16384
	ds_read_b128 v[6:9], v6 offset:20480
	v_or_b32_e32 v50, 32, v170
	v_xad_u32 v40, v50, v48, v49
	ds_read_b128 v[36:39], v40 offset:16384
	s_waitcnt lgkmcnt(2)
	v_mfma_f32_32x32x16_bf16 v[18:33], v[2:5], v[148:151], 0
	s_add_i32 s59, 0, 0x4000
	s_cmp_gt_i32 s40, 3
	v_or_b32_e32 v53, 64, v170
	s_cselect_b64 s[28:29], -1, 0
	s_cmp_lt_i32 s40, 4
	v_and_b32_e32 v52, 0x70, v34
	v_xad_u32 v34, v53, v48, v49
	s_waitcnt lgkmcnt(0)
	v_mfma_f32_32x32x16_bf16 v[18:33], v[36:39], v[152:155], v[18:33]
	ds_read_b128 v[40:43], v40 offset:20480
	ds_read_b128 v[44:47], v34 offset:16384
	s_cselect_b64 s[18:19], -1, 0
	s_lshl_b32 s8, s40, 11
	s_add_u32 s24, s48, s24
	v_add_u32_e32 v38, s59, v35
	v_or_b32_e32 v39, 0x60, v170
	s_addc_u32 s25, s49, s25
	v_xad_u32 v171, v170, v52, v38
	v_xad_u32 v199, v50, v52, v38
	v_xad_u32 v54, v39, v48, v49
	v_xad_u32 v200, v53, v52, v38
	v_xad_u32 v201, v39, v52, v38
	v_lshl_add_u64 v[38:39], s[24:25], 0, v[146:147]
	s_mov_b64 s[24:25], 0x180400
	s_mov_b32 m0, s0
	v_lshl_add_u64 v[38:39], v[38:39], 0, s[24:25]
	ds_read_b128 v[34:37], v34 offset:20480
	ds_read_b128 v[48:51], v54 offset:16384
	s_waitcnt lgkmcnt(2)
	v_mfma_f32_32x32x16_bf16 v[18:33], v[44:47], v[156:159], v[18:33]
	ds_read_b128 v[44:47], v54 offset:20480
	s_waitcnt vmcnt(1)
	s_waitcnt lgkmcnt(0)
	s_barrier
; #define AT_DMA_K(j, so) do { const char* _p = pb + (size_t)__builtin_amdgcn_readfirstlane(AT_ROW(j)) * (INW * 2); \
;         __builtin_amdgcn_global_load_lds((const unsigned*)(_p + dK), (LAS unsigned*)(lds + (so) + SHM_V + widu * 1024), 16, 0, 0); } while (0)
; template <bool ROBUST>
; __device__ __forceinline__ bool attn_pass(const bf16_t* __restrict__ proj, LAS char* lds, int qrow0, int ctxrow0, int latrow0, int NT, int h, int comp, f32x16 (&o)[4]) {
;     ...
;     qkt(pA0, pA1, lds + SHM_V, qr, r32, hi, 0.f); partialSM<true>(pA0, pA1, m_reg, alA);
;     asm volatile("s_waitcnt vmcnt(1)" ::: "memory"); __syncthreads();
;     AT_DMA_K(3, 0);
;     AT_HALF(false, pB0, pB1, pA0, pA1, 1);
	global_load_lds_dwordx4 v[38:39], off
	v_mfma_f32_32x32x16_bf16 v[2:17], v[6:9], v[148:151], 0
	v_add_u32_e32 v52, 0x6000, v199
	v_add_u32_e32 v53, 0x6000, v200
	v_add_u32_e32 v54, 0x6000, v201
	v_mfma_f32_32x32x16_bf16 v[2:17], v[40:43], v[152:155], v[2:17]
	v_add_u32_e32 v42, 0x6000, v171
	v_mfma_f32_32x32x16_bf16 v[18:33], v[48:51], v[160:163], v[18:33]
	v_mfma_f32_32x32x16_bf16 v[2:17], v[34:37], v[156:159], v[2:17]
	s_nop 10
	v_max_f32_e32 v48, v19, v19
	v_max_f32_e32 v49, v18, v18
	v_max_f32_e32 v38, v49, v48
	v_max3_f32 v34, v38, v20, v21
	v_max3_f32 v34, v34, v22, v23
	v_max3_f32 v34, v34, v24, v25
	v_max3_f32 v34, v34, v26, v27
	v_mfma_f32_32x32x16_bf16 v[2:17], v[44:47], v[160:163], v[2:17]
	v_max3_f32 v34, v34, v28, v29
	v_max3_f32 v34, v34, v30, v31
	v_max3_f32 v34, v34, v32, v33
	s_nop 8
	v_max3_f32 v34, v34, v2, v3
	v_max3_f32 v34, v34, v4, v5
	v_max3_f32 v34, v34, v6, v7
	v_max3_f32 v34, v34, v8, v9
	v_max3_f32 v34, v34, v10, v11
	v_max3_f32 v34, v34, v12, v13
	v_max3_f32 v34, v34, v14, v15
	v_max3_f32 v34, v34, v16, v17
	v_mov_b32_e32 v35, v34
	s_nop 1
	v_permlane32_swap_b32_e32 v34, v35
	v_max_f32_e32 v35, v35, v35
	v_max_f32_e32 v34, v34, v34
	v_max_f32_e32 v50, v34, v35
	ds_read_b128 v[34:37], v42 offset:0
	ds_read_b128 v[38:41], v42 offset:0x1000
	ds_read_b128 v[42:45], v52 offset:0
	ds_read_b128 v[46:49], v52 offset:0x1000
	ds_read_b128 v[68:71], v53 offset:0
	ds_read_b128 v[72:75], v53 offset:0x1000
	ds_read_b128 v[76:79], v54 offset:0
	ds_read_b128 v[114:117], v54 offset:0x1000
	v_add_f32_e32 v51, 0, v50
	v_sub_f32_e32 v18, v18, v50
	v_sub_f32_e32 v19, v19, v50
	v_sub_f32_e32 v20, v20, v50
	v_sub_f32_e32 v21, v21, v50
	v_sub_f32_e32 v22, v22, v50
	v_sub_f32_e32 v23, v23, v50
	v_sub_f32_e32 v24, v24, v50
	v_sub_f32_e32 v25, v25, v50
	v_sub_f32_e32 v26, v26, v50
	v_sub_f32_e32 v27, v27, v50
	v_sub_f32_e32 v28, v28, v50
	v_sub_f32_e32 v29, v29, v50
	v_sub_f32_e32 v30, v30, v50
	v_sub_f32_e32 v31, v31, v50
	v_sub_f32_e32 v32, v32, v50
	v_sub_f32_e32 v33, v33, v50
	v_exp_f32_e32 v18, v18
	v_exp_f32_e32 v19, v19
	v_exp_f32_e32 v20, v20
	v_exp_f32_e32 v21, v21
	v_exp_f32_e32 v22, v22
	v_exp_f32_e32 v23, v23
	v_exp_f32_e32 v24, v24
	v_exp_f32_e32 v25, v25
	v_exp_f32_e32 v26, v26
	v_exp_f32_e32 v27, v27
	v_exp_f32_e32 v28, v28
	v_exp_f32_e32 v29, v29
	v_exp_f32_e32 v30, v30
	v_exp_f32_e32 v31, v31
	v_exp_f32_e32 v32, v32
	v_exp_f32_e32 v33, v33
	v_xor_b32_e32 v66, 0x80000000, v51
	v_mov_b32_e32 v82, v66
	v_mov_b32_e32 v83, v66
	v_mov_b32_e32 v84, v66
	v_mov_b32_e32 v85, v66
	v_mov_b32_e32 v86, v66
	v_mov_b32_e32 v87, v66
	v_mov_b32_e32 v88, v66
	v_mov_b32_e32 v89, v66
	v_mov_b32_e32 v90, v66
	v_mov_b32_e32 v91, v66
	v_mov_b32_e32 v92, v66
	v_mov_b32_e32 v93, v66
	v_mov_b32_e32 v94, v66
	v_mov_b32_e32 v95, v66
	v_mov_b32_e32 v96, v66
	v_mov_b32_e32 v97, v66
	v_sub_f32_e32 v2, v2, v50
	v_sub_f32_e32 v3, v3, v50
	v_sub_f32_e32 v4, v4, v50
	v_sub_f32_e32 v5, v5, v50
	v_sub_f32_e32 v6, v6, v50
	v_sub_f32_e32 v7, v7, v50
	v_sub_f32_e32 v8, v8, v50
	v_sub_f32_e32 v9, v9, v50
	v_sub_f32_e32 v10, v10, v50
	v_sub_f32_e32 v11, v11, v50
	v_sub_f32_e32 v12, v12, v50
	v_sub_f32_e32 v13, v13, v50
	v_sub_f32_e32 v14, v14, v50
	v_sub_f32_e32 v15, v15, v50
	v_sub_f32_e32 v16, v16, v50
	v_sub_f32_e32 v17, v17, v50
	s_waitcnt lgkmcnt(6)
	s_waitcnt lgkmcnt(4)
	s_waitcnt lgkmcnt(2)
	v_exp_f32_e32 v2, v2
	v_mfma_f32_32x32x16_bf16 v[50:65], v[34:37], v[148:151], v[82:97]
	v_exp_f32_e32 v3, v3
	v_exp_f32_e32 v4, v4
	v_exp_f32_e32 v5, v5
	v_exp_f32_e32 v10, v10
	v_exp_f32_e32 v11, v11
	v_exp_f32_e32 v12, v12
	v_exp_f32_e32 v13, v13
	v_mfma_f32_32x32x16_bf16 v[98:113], v[38:41], v[148:151], v[82:97]
	v_exp_f32_e32 v6, v6
	v_exp_f32_e32 v7, v7
	v_exp_f32_e32 v14, v14
	v_exp_f32_e32 v15, v15
	v_exp_f32_e32 v8, v8
	v_exp_f32_e32 v9, v9
	v_exp_f32_e32 v16, v16
	v_mfma_f32_32x32x16_bf16 v[50:65], v[42:45], v[152:155], v[50:65]
	v_exp_f32_e32 v17, v17
	s_waitcnt lgkmcnt(0)
	v_pk_add_f32 v[34:35], v[18:19], v[20:21]
	v_pk_add_f32 v[36:37], v[26:27], v[28:29]
	v_pk_add_f32 v[38:39], v[4:5], v[2:3]
	v_pk_add_f32 v[40:41], v[12:13], v[10:11]
	v_pk_add_f32 v[34:35], v[34:35], v[22:23]
	v_mfma_f32_32x32x16_bf16 v[98:113], v[46:49], v[152:155], v[98:113]
	v_add_f32_e64 v36, v36, v30
	v_add_f32_e64 v37, v37, v31
	v_add_f32_e64 v38, v6, v38
	v_add_f32_e64 v39, v7, v39
	v_add_f32_e64 v40, v14, v40
	v_add_f32_e64 v41, v15, v41
	v_pk_add_f32 v[34:35], v[34:35], v[24:25]
	v_pk_add_f32 v[36:37], v[36:37], v[32:33]
	v_pk_add_f32 v[38:39], v[8:9], v[38:39]
	v_pk_add_f32 v[40:41], v[16:17], v[40:41]
	v_mfma_f32_32x32x16_bf16 v[50:65], v[68:71], v[156:159], v[50:65]
	v_add_f32_e64 v34, v34, v36
	v_add_f32_e64 v35, v35, v37
	v_add_f32_e64 v36, v38, v40
	v_add_f32_e64 v37, v39, v41
	v_add_f32_e64 v34, v36, v34
	v_add_f32_e64 v35, v37, v35
	v_pk_add_f32 v[174:175], v[34:35], v[34:35] op_sel:[0,1] op_sel_hi:[1,0]
	v_mfma_f32_32x32x16_bf16 v[98:113], v[72:75], v[156:159], v[98:113]
	v_mov_b32_e32 v175, v174
	s_nop 1
	v_permlane32_swap_b32_e32 v174, v175
	v_cvt_pk_bf16_f32 v72, v18, v19
	v_cvt_pk_bf16_f32 v73, v20, v21
	v_cvt_pk_bf16_f32 v74, v22, v23
	v_cvt_pk_bf16_f32 v75, v24, v25
	v_mfma_f32_32x32x16_bf16 v[50:65], v[76:79], v[160:163], v[50:65]
	v_cvt_pk_bf16_f32 v68, v26, v27
	v_cvt_pk_bf16_f32 v69, v28, v29
	v_cvt_pk_bf16_f32 v70, v30, v31
	v_cvt_pk_bf16_f32 v71, v32, v33
	v_cvt_pk_bf16_f32 v76, v2, v3
	v_cvt_pk_bf16_f32 v77, v4, v5
	v_cvt_pk_bf16_f32 v78, v6, v7
	v_mfma_f32_32x32x16_bf16 v[98:113], v[114:117], v[160:163], v[98:113]
	v_cvt_pk_bf16_f32 v79, v8, v9
	v_cvt_pk_bf16_f32 v114, v10, v11
	v_cvt_pk_bf16_f32 v115, v12, v13
	v_cvt_pk_bf16_f32 v116, v14, v15
	v_cvt_pk_bf16_f32 v117, v16, v17
	v_cndmask_b32_e64 v2, 0, 1, s[50:51]
	s_and_b64 vcc, exec, s[18:19]
	v_cmp_ne_u32_e64 s[44:45], 1, v2
	s_mov_b64 s[82:83], 0x100000
	s_cbranch_vccnz .LBB0_353
	s_lshl_b64 s[24:25], s[70:71], 13
	s_add_u32 s24, s48, s24
	s_addc_u32 s25, s49, s25
	v_lshl_add_u64 v[2:3], s[24:25], 0, v[172:173]
	s_add_i32 s9, s8, 0
	v_lshl_add_u64 v[4:5], v[2:3], 0, s[38:39]
	s_add_i32 m0, s9, 0xc000
	s_waitcnt vmcnt(1) lgkmcnt(0)
	s_barrier
	global_load_lds_dwordx4 v[4:5], off
	v_lshl_add_u64 v[2:3], v[2:3], 0, s[4:5]
	s_add_i32 m0, s9, 0xc400
	s_and_b64 vcc, exec, s[44:45]
	global_load_lds_dwordx4 v[2:3], off
	s_cbranch_vccnz .LBB0_353
	s_ashr_i32 s55, s54, 31
	s_lshl_b64 s[24:25], s[54:55], 13
	s_add_u32 s24, s48, s24
	s_addc_u32 s25, s49, s25
	v_lshl_add_u64 v[2:3], s[24:25], 0, v[146:147]
	v_lshl_add_u64 v[2:3], v[2:3], 0, s[10:11]
	s_mov_b32 m0, s42
	s_nop 0
	global_load_lds_dwordx4 v[2:3], off
